# prologue adaLN modulation GEMV: SiLU scalars once per wave + 16-row register ring with counted vmcnt waits (was 1 row in flight per wave)
# speedup vs baseline: 1.0082x; 1.0026x over previous
.Lmodk_start:
	s_waitcnt vmcnt(0)
	v_add_co_u32_e32 v114, vcc, 0xfffa0000, v14
	s_nop 1
	v_addc_co_u32_e32 v115, vcc, -1, v15, vcc
	v_and_b32_e32 v116, 63, v0
	v_lshlrev_b32_e32 v116, 4, v116
	v_mov_b32_e32 v117, 0
	v_lshl_add_u64 v[126:127], v[16:17], 0, v[116:117]
	v_lshl_add_u64 v[128:129], v[20:21], 0, v[126:127]
	v_lshl_add_u64 v[130:131], v[18:19], 0, v[126:127]
	global_load_dwordx4 v[118:121], v[128:129], off
	global_load_dwordx4 v[122:125], v[130:131], off
	s_mov_b32 s24, 0xc000
	s_mov_b32 s25, 0
	global_load_dwordx4 v[14:17], v[114:115], off
	v_lshl_add_u64 v[114:115], v[114:115], 0, s[24:25]
	global_load_dwordx4 v[18:21], v[114:115], off
	v_lshl_add_u64 v[114:115], v[114:115], 0, s[24:25]
	global_load_dwordx4 v[22:25], v[114:115], off
	v_lshl_add_u64 v[114:115], v[114:115], 0, s[24:25]
	global_load_dwordx4 v[26:29], v[114:115], off
	v_lshl_add_u64 v[114:115], v[114:115], 0, s[24:25]
	global_load_dwordx4 v[30:33], v[114:115], off
	v_lshl_add_u64 v[114:115], v[114:115], 0, s[24:25]
	global_load_dwordx4 v[34:37], v[114:115], off
	v_lshl_add_u64 v[114:115], v[114:115], 0, s[24:25]
	global_load_dwordx4 v[38:41], v[114:115], off
	v_lshl_add_u64 v[114:115], v[114:115], 0, s[24:25]
	global_load_dwordx4 v[42:45], v[114:115], off
	v_lshl_add_u64 v[114:115], v[114:115], 0, s[24:25]
	global_load_dwordx4 v[46:49], v[114:115], off
	v_lshl_add_u64 v[114:115], v[114:115], 0, s[24:25]
	global_load_dwordx4 v[50:53], v[114:115], off
	v_lshl_add_u64 v[114:115], v[114:115], 0, s[24:25]
	global_load_dwordx4 v[54:57], v[114:115], off
	v_lshl_add_u64 v[114:115], v[114:115], 0, s[24:25]
	global_load_dwordx4 v[58:61], v[114:115], off
	v_lshl_add_u64 v[114:115], v[114:115], 0, s[24:25]
	global_load_dwordx4 v[62:65], v[114:115], off
	v_lshl_add_u64 v[114:115], v[114:115], 0, s[24:25]
	global_load_dwordx4 v[66:69], v[114:115], off
	v_lshl_add_u64 v[114:115], v[114:115], 0, s[24:25]
	global_load_dwordx4 v[70:73], v[114:115], off
	v_lshl_add_u64 v[114:115], v[114:115], 0, s[24:25]
	global_load_dwordx4 v[74:77], v[114:115], off
	v_lshl_add_u64 v[114:115], v[114:115], 0, s[24:25]
	s_waitcnt vmcnt(16)
	v_mul_f32_e32 v132, 0xbfb8aa3b, v118
	v_exp_f32_e32 v132, v132
	s_nop 0
	v_add_f32_e32 v133, 1.0, v132
	v_div_scale_f32 v134, s[6:7], v133, v133, v118
	v_div_scale_f32 v135, vcc, v118, v133, v118
	v_rcp_f32_e32 v136, v134
	s_nop 0
	v_fma_f32 v132, -v134, v136, 1.0
	v_fmac_f32_e32 v136, v132, v136
	v_mul_f32_e32 v137, v135, v136
	v_fma_f32 v132, -v134, v137, v135
	v_fmac_f32_e32 v137, v132, v136
	v_fma_f32 v132, -v134, v137, v135
	v_div_fmas_f32 v132, v132, v136, v137
	v_div_fixup_f32 v118, v132, v133, v118
	v_mul_f32_e32 v132, 0xbfb8aa3b, v119
	v_exp_f32_e32 v132, v132
	s_nop 0
	v_add_f32_e32 v133, 1.0, v132
	v_div_scale_f32 v134, s[6:7], v133, v133, v119
	v_div_scale_f32 v135, vcc, v119, v133, v119
	v_rcp_f32_e32 v136, v134
	s_nop 0
	v_fma_f32 v132, -v134, v136, 1.0
	v_fmac_f32_e32 v136, v132, v136
	v_mul_f32_e32 v137, v135, v136
	v_fma_f32 v132, -v134, v137, v135
	v_fmac_f32_e32 v137, v132, v136
	v_fma_f32 v132, -v134, v137, v135
	v_div_fmas_f32 v132, v132, v136, v137
	v_div_fixup_f32 v119, v132, v133, v119
	v_mul_f32_e32 v132, 0xbfb8aa3b, v120
	v_exp_f32_e32 v132, v132
	s_nop 0
	v_add_f32_e32 v133, 1.0, v132
	v_div_scale_f32 v134, s[6:7], v133, v133, v120
	v_div_scale_f32 v135, vcc, v120, v133, v120
	v_rcp_f32_e32 v136, v134
	s_nop 0
	v_fma_f32 v132, -v134, v136, 1.0
	v_fmac_f32_e32 v136, v132, v136
	v_mul_f32_e32 v137, v135, v136
	v_fma_f32 v132, -v134, v137, v135
	v_fmac_f32_e32 v137, v132, v136
	v_fma_f32 v132, -v134, v137, v135
	v_div_fmas_f32 v132, v132, v136, v137
	v_div_fixup_f32 v120, v132, v133, v120
	v_mul_f32_e32 v132, 0xbfb8aa3b, v121
	v_exp_f32_e32 v132, v132
	s_nop 0
	v_add_f32_e32 v133, 1.0, v132
	v_div_scale_f32 v134, s[6:7], v133, v133, v121
	v_div_scale_f32 v135, vcc, v121, v133, v121
	v_rcp_f32_e32 v136, v134
	s_nop 0
	v_fma_f32 v132, -v134, v136, 1.0
	v_fmac_f32_e32 v136, v132, v136
	v_mul_f32_e32 v137, v135, v136
	v_fma_f32 v132, -v134, v137, v135
	v_fmac_f32_e32 v137, v132, v136
	v_fma_f32 v132, -v134, v137, v135
	v_div_fmas_f32 v132, v132, v136, v137
	v_div_fixup_f32 v121, v132, v133, v121
	v_mul_f32_e32 v132, 0xbfb8aa3b, v122
	v_exp_f32_e32 v132, v132
	s_nop 0
	v_add_f32_e32 v133, 1.0, v132
	v_div_scale_f32 v134, s[6:7], v133, v133, v122
	v_div_scale_f32 v135, vcc, v122, v133, v122
	v_rcp_f32_e32 v136, v134
	s_nop 0
	v_fma_f32 v132, -v134, v136, 1.0
	v_fmac_f32_e32 v136, v132, v136
	v_mul_f32_e32 v137, v135, v136
	v_fma_f32 v132, -v134, v137, v135
	v_fmac_f32_e32 v137, v132, v136
	v_fma_f32 v132, -v134, v137, v135
	v_div_fmas_f32 v132, v132, v136, v137
	v_div_fixup_f32 v122, v132, v133, v122
	v_mul_f32_e32 v132, 0xbfb8aa3b, v123
	v_exp_f32_e32 v132, v132
	s_nop 0
	v_add_f32_e32 v133, 1.0, v132
	v_div_scale_f32 v134, s[6:7], v133, v133, v123
	v_div_scale_f32 v135, vcc, v123, v133, v123
	v_rcp_f32_e32 v136, v134
	s_nop 0
	v_fma_f32 v132, -v134, v136, 1.0
	v_fmac_f32_e32 v136, v132, v136
	v_mul_f32_e32 v137, v135, v136
	v_fma_f32 v132, -v134, v137, v135
	v_fmac_f32_e32 v137, v132, v136
	v_fma_f32 v132, -v134, v137, v135
	v_div_fmas_f32 v132, v132, v136, v137
	v_div_fixup_f32 v123, v132, v133, v123
	v_mul_f32_e32 v132, 0xbfb8aa3b, v124
	v_exp_f32_e32 v132, v132
	s_nop 0
	v_add_f32_e32 v133, 1.0, v132
	v_div_scale_f32 v134, s[6:7], v133, v133, v124
	v_div_scale_f32 v135, vcc, v124, v133, v124
	v_rcp_f32_e32 v136, v134
	s_nop 0
	v_fma_f32 v132, -v134, v136, 1.0
	v_fmac_f32_e32 v136, v132, v136
	v_mul_f32_e32 v137, v135, v136
	v_fma_f32 v132, -v134, v137, v135
	v_fmac_f32_e32 v137, v132, v136
	v_fma_f32 v132, -v134, v137, v135
	v_div_fmas_f32 v132, v132, v136, v137
	v_div_fixup_f32 v124, v132, v133, v124
	v_mul_f32_e32 v132, 0xbfb8aa3b, v125
	v_exp_f32_e32 v132, v132
	s_nop 0
	v_add_f32_e32 v133, 1.0, v132
	v_div_scale_f32 v134, s[6:7], v133, v133, v125
	v_div_scale_f32 v135, vcc, v125, v133, v125
	v_rcp_f32_e32 v136, v134
	s_nop 0
	v_fma_f32 v132, -v134, v136, 1.0
	v_fmac_f32_e32 v136, v132, v136
	v_mul_f32_e32 v137, v135, v136
	v_fma_f32 v132, -v134, v137, v135
	v_fmac_f32_e32 v137, v132, v136
	v_fma_f32 v132, -v134, v137, v135
	v_div_fmas_f32 v132, v132, v136, v137
	v_div_fixup_f32 v125, v132, v133, v125
	s_mov_b32 s26, 0
.Lmodk_loop:
	s_lshl_b32 s28, s26, 2
	s_add_i32 s29, s28, 1
	s_add_i32 s30, s28, 2
	s_add_i32 s31, s28, 3
	s_add_i32 s26, s26, 1
	s_nop 1
	v_readlane_b32 s4, v118, s28
	v_readlane_b32 s5, v122, s28
	v_readlane_b32 s6, v119, s28
	v_readlane_b32 s7, v123, s28
	v_readlane_b32 s10, v120, s28
	v_readlane_b32 s11, v124, s28
	v_readlane_b32 s34, v121, s28
	v_readlane_b32 s35, v125, s28
	s_waitcnt vmcnt(15)
	v_fmac_f32_e32 v2, s4, v14
	v_fmac_f32_e32 v3, s4, v15
	v_fmac_f32_e32 v4, s4, v16
	v_fmac_f32_e32 v5, s4, v17
	v_fmac_f32_e32 v6, s5, v14
	v_fmac_f32_e32 v7, s5, v15
	v_fmac_f32_e32 v8, s5, v16
	v_fmac_f32_e32 v9, s5, v17
	global_load_dwordx4 v[14:17], v[114:115], off
	v_lshl_add_u64 v[114:115], v[114:115], 0, s[24:25]
	s_waitcnt vmcnt(15)
	v_fmac_f32_e32 v2, s6, v18
	v_fmac_f32_e32 v3, s6, v19
	v_fmac_f32_e32 v4, s6, v20
	v_fmac_f32_e32 v5, s6, v21
	v_fmac_f32_e32 v6, s7, v18
	v_fmac_f32_e32 v7, s7, v19
	v_fmac_f32_e32 v8, s7, v20
	v_fmac_f32_e32 v9, s7, v21
	global_load_dwordx4 v[18:21], v[114:115], off
	v_lshl_add_u64 v[114:115], v[114:115], 0, s[24:25]
	s_waitcnt vmcnt(15)
	v_fmac_f32_e32 v2, s10, v22
	v_fmac_f32_e32 v3, s10, v23
	v_fmac_f32_e32 v4, s10, v24
	v_fmac_f32_e32 v5, s10, v25
	v_fmac_f32_e32 v6, s11, v22
	v_fmac_f32_e32 v7, s11, v23
	v_fmac_f32_e32 v8, s11, v24
	v_fmac_f32_e32 v9, s11, v25
	global_load_dwordx4 v[22:25], v[114:115], off
	v_lshl_add_u64 v[114:115], v[114:115], 0, s[24:25]
	s_waitcnt vmcnt(15)
	v_fmac_f32_e32 v2, s34, v26
	v_fmac_f32_e32 v3, s34, v27
	v_fmac_f32_e32 v4, s34, v28
	v_fmac_f32_e32 v5, s34, v29
	v_fmac_f32_e32 v6, s35, v26
	v_fmac_f32_e32 v7, s35, v27
	v_fmac_f32_e32 v8, s35, v28
	v_fmac_f32_e32 v9, s35, v29
	global_load_dwordx4 v[26:29], v[114:115], off
	v_lshl_add_u64 v[114:115], v[114:115], 0, s[24:25]
	v_readlane_b32 s4, v118, s29
	v_readlane_b32 s5, v122, s29
	v_readlane_b32 s6, v119, s29
	v_readlane_b32 s7, v123, s29
	v_readlane_b32 s10, v120, s29
	v_readlane_b32 s11, v124, s29
	v_readlane_b32 s34, v121, s29
	v_readlane_b32 s35, v125, s29
	s_waitcnt vmcnt(15)
	v_fmac_f32_e32 v2, s4, v30
	v_fmac_f32_e32 v3, s4, v31
	v_fmac_f32_e32 v4, s4, v32
	v_fmac_f32_e32 v5, s4, v33
	v_fmac_f32_e32 v6, s5, v30
	v_fmac_f32_e32 v7, s5, v31
	v_fmac_f32_e32 v8, s5, v32
	v_fmac_f32_e32 v9, s5, v33
	global_load_dwordx4 v[30:33], v[114:115], off
	v_lshl_add_u64 v[114:115], v[114:115], 0, s[24:25]
	s_waitcnt vmcnt(15)
	v_fmac_f32_e32 v2, s6, v34
	v_fmac_f32_e32 v3, s6, v35
	v_fmac_f32_e32 v4, s6, v36
	v_fmac_f32_e32 v5, s6, v37
	v_fmac_f32_e32 v6, s7, v34
	v_fmac_f32_e32 v7, s7, v35
	v_fmac_f32_e32 v8, s7, v36
	v_fmac_f32_e32 v9, s7, v37
	global_load_dwordx4 v[34:37], v[114:115], off
	v_lshl_add_u64 v[114:115], v[114:115], 0, s[24:25]
	s_waitcnt vmcnt(15)
	v_fmac_f32_e32 v2, s10, v38
	v_fmac_f32_e32 v3, s10, v39
	v_fmac_f32_e32 v4, s10, v40
	v_fmac_f32_e32 v5, s10, v41
	v_fmac_f32_e32 v6, s11, v38
	v_fmac_f32_e32 v7, s11, v39
	v_fmac_f32_e32 v8, s11, v40
	v_fmac_f32_e32 v9, s11, v41
	global_load_dwordx4 v[38:41], v[114:115], off
	v_lshl_add_u64 v[114:115], v[114:115], 0, s[24:25]
	s_waitcnt vmcnt(15)
	v_fmac_f32_e32 v2, s34, v42
	v_fmac_f32_e32 v3, s34, v43
	v_fmac_f32_e32 v4, s34, v44
	v_fmac_f32_e32 v5, s34, v45
	v_fmac_f32_e32 v6, s35, v42
	v_fmac_f32_e32 v7, s35, v43
	v_fmac_f32_e32 v8, s35, v44
	v_fmac_f32_e32 v9, s35, v45
	global_load_dwordx4 v[42:45], v[114:115], off
	v_lshl_add_u64 v[114:115], v[114:115], 0, s[24:25]
	v_readlane_b32 s4, v118, s30
	v_readlane_b32 s5, v122, s30
	v_readlane_b32 s6, v119, s30
	v_readlane_b32 s7, v123, s30
	v_readlane_b32 s10, v120, s30
	v_readlane_b32 s11, v124, s30
	v_readlane_b32 s34, v121, s30
	v_readlane_b32 s35, v125, s30
	s_waitcnt vmcnt(15)
	v_fmac_f32_e32 v2, s4, v46
	v_fmac_f32_e32 v3, s4, v47
	v_fmac_f32_e32 v4, s4, v48
	v_fmac_f32_e32 v5, s4, v49
	v_fmac_f32_e32 v6, s5, v46
	v_fmac_f32_e32 v7, s5, v47
	v_fmac_f32_e32 v8, s5, v48
	v_fmac_f32_e32 v9, s5, v49
	global_load_dwordx4 v[46:49], v[114:115], off
	v_lshl_add_u64 v[114:115], v[114:115], 0, s[24:25]
	s_waitcnt vmcnt(15)
	v_fmac_f32_e32 v2, s6, v50
	v_fmac_f32_e32 v3, s6, v51
	v_fmac_f32_e32 v4, s6, v52
	v_fmac_f32_e32 v5, s6, v53
	v_fmac_f32_e32 v6, s7, v50
	v_fmac_f32_e32 v7, s7, v51
	v_fmac_f32_e32 v8, s7, v52
	v_fmac_f32_e32 v9, s7, v53
	global_load_dwordx4 v[50:53], v[114:115], off
	v_lshl_add_u64 v[114:115], v[114:115], 0, s[24:25]
	s_waitcnt vmcnt(15)
	v_fmac_f32_e32 v2, s10, v54
	v_fmac_f32_e32 v3, s10, v55
	v_fmac_f32_e32 v4, s10, v56
	v_fmac_f32_e32 v5, s10, v57
	v_fmac_f32_e32 v6, s11, v54
	v_fmac_f32_e32 v7, s11, v55
	v_fmac_f32_e32 v8, s11, v56
	v_fmac_f32_e32 v9, s11, v57
	global_load_dwordx4 v[54:57], v[114:115], off
	v_lshl_add_u64 v[114:115], v[114:115], 0, s[24:25]
	s_waitcnt vmcnt(15)
	v_fmac_f32_e32 v2, s34, v58
	v_fmac_f32_e32 v3, s34, v59
	v_fmac_f32_e32 v4, s34, v60
	v_fmac_f32_e32 v5, s34, v61
	v_fmac_f32_e32 v6, s35, v58
	v_fmac_f32_e32 v7, s35, v59
	v_fmac_f32_e32 v8, s35, v60
	v_fmac_f32_e32 v9, s35, v61
	global_load_dwordx4 v[58:61], v[114:115], off
	v_lshl_add_u64 v[114:115], v[114:115], 0, s[24:25]
	v_readlane_b32 s4, v118, s31
	v_readlane_b32 s5, v122, s31
	v_readlane_b32 s6, v119, s31
	v_readlane_b32 s7, v123, s31
	v_readlane_b32 s10, v120, s31
	v_readlane_b32 s11, v124, s31
	v_readlane_b32 s34, v121, s31
	v_readlane_b32 s35, v125, s31
	s_waitcnt vmcnt(15)
	v_fmac_f32_e32 v2, s4, v62
	v_fmac_f32_e32 v3, s4, v63
	v_fmac_f32_e32 v4, s4, v64
	v_fmac_f32_e32 v5, s4, v65
	v_fmac_f32_e32 v6, s5, v62
	v_fmac_f32_e32 v7, s5, v63
	v_fmac_f32_e32 v8, s5, v64
	v_fmac_f32_e32 v9, s5, v65
	global_load_dwordx4 v[62:65], v[114:115], off
	v_lshl_add_u64 v[114:115], v[114:115], 0, s[24:25]
	s_waitcnt vmcnt(15)
	v_fmac_f32_e32 v2, s6, v66
	v_fmac_f32_e32 v3, s6, v67
	v_fmac_f32_e32 v4, s6, v68
	v_fmac_f32_e32 v5, s6, v69
	v_fmac_f32_e32 v6, s7, v66
	v_fmac_f32_e32 v7, s7, v67
	v_fmac_f32_e32 v8, s7, v68
	v_fmac_f32_e32 v9, s7, v69
	global_load_dwordx4 v[66:69], v[114:115], off
	v_lshl_add_u64 v[114:115], v[114:115], 0, s[24:25]
	s_waitcnt vmcnt(15)
	v_fmac_f32_e32 v2, s10, v70
	v_fmac_f32_e32 v3, s10, v71
	v_fmac_f32_e32 v4, s10, v72
	v_fmac_f32_e32 v5, s10, v73
	v_fmac_f32_e32 v6, s11, v70
	v_fmac_f32_e32 v7, s11, v71
	v_fmac_f32_e32 v8, s11, v72
	v_fmac_f32_e32 v9, s11, v73
	global_load_dwordx4 v[70:73], v[114:115], off
	v_lshl_add_u64 v[114:115], v[114:115], 0, s[24:25]
	s_waitcnt vmcnt(15)
	v_fmac_f32_e32 v2, s34, v74
	v_fmac_f32_e32 v3, s34, v75
	v_fmac_f32_e32 v4, s34, v76
	v_fmac_f32_e32 v5, s34, v77
	v_fmac_f32_e32 v6, s35, v74
	v_fmac_f32_e32 v7, s35, v75
	v_fmac_f32_e32 v8, s35, v76
	v_fmac_f32_e32 v9, s35, v77
	global_load_dwordx4 v[74:77], v[114:115], off
	v_lshl_add_u64 v[114:115], v[114:115], 0, s[24:25]
	s_cmp_lt_u32 s26, 15
	s_cbranch_scc1 .Lmodk_loop
	v_readlane_b32 s4, v118, 60
	v_readlane_b32 s5, v122, 60
	v_readlane_b32 s6, v119, 60
	v_readlane_b32 s7, v123, 60
	v_readlane_b32 s10, v120, 60
	v_readlane_b32 s11, v124, 60
	v_readlane_b32 s34, v121, 60
	v_readlane_b32 s35, v125, 60
	s_waitcnt vmcnt(15)
	v_fmac_f32_e32 v2, s4, v14
	v_fmac_f32_e32 v3, s4, v15
	v_fmac_f32_e32 v4, s4, v16
	v_fmac_f32_e32 v5, s4, v17
	v_fmac_f32_e32 v6, s5, v14
	v_fmac_f32_e32 v7, s5, v15
	v_fmac_f32_e32 v8, s5, v16
	v_fmac_f32_e32 v9, s5, v17
	s_waitcnt vmcnt(14)
	v_fmac_f32_e32 v2, s6, v18
	v_fmac_f32_e32 v3, s6, v19
	v_fmac_f32_e32 v4, s6, v20
	v_fmac_f32_e32 v5, s6, v21
	v_fmac_f32_e32 v6, s7, v18
	v_fmac_f32_e32 v7, s7, v19
	v_fmac_f32_e32 v8, s7, v20
	v_fmac_f32_e32 v9, s7, v21
	s_waitcnt vmcnt(13)
	v_fmac_f32_e32 v2, s10, v22
	v_fmac_f32_e32 v3, s10, v23
	v_fmac_f32_e32 v4, s10, v24
	v_fmac_f32_e32 v5, s10, v25
	v_fmac_f32_e32 v6, s11, v22
	v_fmac_f32_e32 v7, s11, v23
	v_fmac_f32_e32 v8, s11, v24
	v_fmac_f32_e32 v9, s11, v25
	s_waitcnt vmcnt(12)
	v_fmac_f32_e32 v2, s34, v26
	v_fmac_f32_e32 v3, s34, v27
	v_fmac_f32_e32 v4, s34, v28
	v_fmac_f32_e32 v5, s34, v29
	v_fmac_f32_e32 v6, s35, v26
	v_fmac_f32_e32 v7, s35, v27
	v_fmac_f32_e32 v8, s35, v28
	v_fmac_f32_e32 v9, s35, v29
	v_readlane_b32 s4, v118, 61
	v_readlane_b32 s5, v122, 61
	v_readlane_b32 s6, v119, 61
	v_readlane_b32 s7, v123, 61
	v_readlane_b32 s10, v120, 61
	v_readlane_b32 s11, v124, 61
	v_readlane_b32 s34, v121, 61
	v_readlane_b32 s35, v125, 61
	s_waitcnt vmcnt(11)
	v_fmac_f32_e32 v2, s4, v30
	v_fmac_f32_e32 v3, s4, v31
	v_fmac_f32_e32 v4, s4, v32
	v_fmac_f32_e32 v5, s4, v33
	v_fmac_f32_e32 v6, s5, v30
	v_fmac_f32_e32 v7, s5, v31
	v_fmac_f32_e32 v8, s5, v32
	v_fmac_f32_e32 v9, s5, v33
	s_waitcnt vmcnt(10)
	v_fmac_f32_e32 v2, s6, v34
	v_fmac_f32_e32 v3, s6, v35
	v_fmac_f32_e32 v4, s6, v36
	v_fmac_f32_e32 v5, s6, v37
	v_fmac_f32_e32 v6, s7, v34
	v_fmac_f32_e32 v7, s7, v35
	v_fmac_f32_e32 v8, s7, v36
	v_fmac_f32_e32 v9, s7, v37
	s_waitcnt vmcnt(9)
	v_fmac_f32_e32 v2, s10, v38
	v_fmac_f32_e32 v3, s10, v39
	v_fmac_f32_e32 v4, s10, v40
	v_fmac_f32_e32 v5, s10, v41
	v_fmac_f32_e32 v6, s11, v38
	v_fmac_f32_e32 v7, s11, v39
	v_fmac_f32_e32 v8, s11, v40
	v_fmac_f32_e32 v9, s11, v41
	s_waitcnt vmcnt(8)
	v_fmac_f32_e32 v2, s34, v42
	v_fmac_f32_e32 v3, s34, v43
	v_fmac_f32_e32 v4, s34, v44
	v_fmac_f32_e32 v5, s34, v45
	v_fmac_f32_e32 v6, s35, v42
	v_fmac_f32_e32 v7, s35, v43
	v_fmac_f32_e32 v8, s35, v44
	v_fmac_f32_e32 v9, s35, v45
	v_readlane_b32 s4, v118, 62
	v_readlane_b32 s5, v122, 62
	v_readlane_b32 s6, v119, 62
	v_readlane_b32 s7, v123, 62
	v_readlane_b32 s10, v120, 62
	v_readlane_b32 s11, v124, 62
	v_readlane_b32 s34, v121, 62
	v_readlane_b32 s35, v125, 62
	s_waitcnt vmcnt(7)
	v_fmac_f32_e32 v2, s4, v46
	v_fmac_f32_e32 v3, s4, v47
	v_fmac_f32_e32 v4, s4, v48
	v_fmac_f32_e32 v5, s4, v49
	v_fmac_f32_e32 v6, s5, v46
	v_fmac_f32_e32 v7, s5, v47
	v_fmac_f32_e32 v8, s5, v48
	v_fmac_f32_e32 v9, s5, v49
	s_waitcnt vmcnt(6)
	v_fmac_f32_e32 v2, s6, v50
	v_fmac_f32_e32 v3, s6, v51
	v_fmac_f32_e32 v4, s6, v52
	v_fmac_f32_e32 v5, s6, v53
	v_fmac_f32_e32 v6, s7, v50
	v_fmac_f32_e32 v7, s7, v51
	v_fmac_f32_e32 v8, s7, v52
	v_fmac_f32_e32 v9, s7, v53
	s_waitcnt vmcnt(5)
	v_fmac_f32_e32 v2, s10, v54
	v_fmac_f32_e32 v3, s10, v55
	v_fmac_f32_e32 v4, s10, v56
	v_fmac_f32_e32 v5, s10, v57
	v_fmac_f32_e32 v6, s11, v54
	v_fmac_f32_e32 v7, s11, v55
	v_fmac_f32_e32 v8, s11, v56
	v_fmac_f32_e32 v9, s11, v57
	s_waitcnt vmcnt(4)
	v_fmac_f32_e32 v2, s34, v58
	v_fmac_f32_e32 v3, s34, v59
	v_fmac_f32_e32 v4, s34, v60
	v_fmac_f32_e32 v5, s34, v61
	v_fmac_f32_e32 v6, s35, v58
	v_fmac_f32_e32 v7, s35, v59
	v_fmac_f32_e32 v8, s35, v60
	v_fmac_f32_e32 v9, s35, v61
	v_readlane_b32 s4, v118, 63
	v_readlane_b32 s5, v122, 63
	v_readlane_b32 s6, v119, 63
	v_readlane_b32 s7, v123, 63
	v_readlane_b32 s10, v120, 63
	v_readlane_b32 s11, v124, 63
	v_readlane_b32 s34, v121, 63
	v_readlane_b32 s35, v125, 63
	s_waitcnt vmcnt(3)
	v_fmac_f32_e32 v2, s4, v62
	v_fmac_f32_e32 v3, s4, v63
	v_fmac_f32_e32 v4, s4, v64
	v_fmac_f32_e32 v5, s4, v65
	v_fmac_f32_e32 v6, s5, v62
	v_fmac_f32_e32 v7, s5, v63
	v_fmac_f32_e32 v8, s5, v64
	v_fmac_f32_e32 v9, s5, v65
	s_waitcnt vmcnt(2)
	v_fmac_f32_e32 v2, s6, v66
	v_fmac_f32_e32 v3, s6, v67
	v_fmac_f32_e32 v4, s6, v68
	v_fmac_f32_e32 v5, s6, v69
	v_fmac_f32_e32 v6, s7, v66
	v_fmac_f32_e32 v7, s7, v67
	v_fmac_f32_e32 v8, s7, v68
	v_fmac_f32_e32 v9, s7, v69
	s_waitcnt vmcnt(1)
	v_fmac_f32_e32 v2, s10, v70
	v_fmac_f32_e32 v3, s10, v71
	v_fmac_f32_e32 v4, s10, v72
	v_fmac_f32_e32 v5, s10, v73
	v_fmac_f32_e32 v6, s11, v70
	v_fmac_f32_e32 v7, s11, v71
	v_fmac_f32_e32 v8, s11, v72
	v_fmac_f32_e32 v9, s11, v73
	s_waitcnt vmcnt(0)
	v_fmac_f32_e32 v2, s34, v74
	v_fmac_f32_e32 v3, s34, v75
	v_fmac_f32_e32 v4, s34, v76
	v_fmac_f32_e32 v5, s34, v77
	v_fmac_f32_e32 v6, s35, v74
	v_fmac_f32_e32 v7, s35, v75
	v_fmac_f32_e32 v8, s35, v76
	v_fmac_f32_e32 v9, s35, v77
